# speedup vs baseline: 1.0753x; 1.0053x over previous
.LBB0_12:
	s_or_b64 exec, exec, s[4:5]
	v_mov_b32_e32 v29, 1
	s_waitcnt lgkmcnt(0)
	s_barrier
	ds_add_rtn_u32 v31, v35, v29
	s_mov_b32 s3, 0xff3c
	v_mad_u64_u32 v[32:33], s[4:5], v26, s3, v[12:13]
	v_lshl_or_b32 v12, v32, 16, v13
	s_waitcnt lgkmcnt(0)
	v_lshlrev_b32_e32 v13, 2, v31
	ds_write_b32 v13, v12
	ds_add_rtn_u32 v26, v34, v29
	v_mad_u64_u32 v[12:13], s[4:5], v25, s3, v[14:15]
	v_lshl_or_b32 v12, v12, 16, v15
	v_lshl_add_u64 v[2:3], v[2:3], 2, s[6:7]
	s_waitcnt lgkmcnt(0)
	v_lshlrev_b32_e32 v13, 2, v26
	ds_write_b32 v13, v12
	ds_add_rtn_u32 v14, v30, v29
	v_mad_u64_u32 v[12:13], s[4:5], v24, s3, v[16:17]
	v_lshl_or_b32 v12, v12, 16, v17
	v_lshl_add_u64 v[4:5], v[4:5], 2, s[6:7]
	s_waitcnt lgkmcnt(0)
	v_lshlrev_b32_e32 v13, 2, v14
	ds_write_b32 v13, v12
	ds_add_rtn_u32 v14, v28, v29
	v_mad_u64_u32 v[12:13], s[4:5], v23, s3, v[18:19]
	v_lshl_or_b32 v12, v12, 16, v19
	s_waitcnt lgkmcnt(0)
	v_lshlrev_b32_e32 v13, 2, v14
	ds_write_b32 v13, v12
	ds_add_rtn_u32 v14, v27, v29
	v_mad_u64_u32 v[12:13], s[4:5], v22, s3, v[20:21]
	v_lshl_or_b32 v12, v12, 16, v21
	s_mov_b64 s[4:5], 0
	s_waitcnt lgkmcnt(0)
	v_lshlrev_b32_e32 v13, 2, v14
	ds_write_b32 v13, v12
	s_waitcnt lgkmcnt(0)
	s_barrier
	ds_read2st64_b32 v[12:13], v1 offset1:16
	s_waitcnt lgkmcnt(0)
	global_store_dword v[2:3], v12, off sc1
	ds_read2st64_b32 v[2:3], v1 offset0:32 offset1:48
	ds_read_b32 v1, v1 offset:16384
	global_store_dword v[4:5], v13, off sc1
	v_lshl_add_u64 v[4:5], v[6:7], 2, s[6:7]
	s_waitcnt lgkmcnt(1)
	global_store_dword v[4:5], v2, off sc1
	v_lshl_add_u64 v[4:5], v[8:9], 2, s[6:7]
	global_store_dword v[4:5], v3, off sc1
	v_lshl_add_u64 v[2:3], v[10:11], 2, s[6:7]
	s_waitcnt lgkmcnt(0)
	global_store_dword v[2:3], v1, off sc1

.LBB1_69:
	ds_read_b32 v27, v21
	v_add_u32_e32 v18, v30, v0
	v_add_u32_e32 v0, 0x400, v0
	v_cmp_ge_u32_e32 vcc, v0, v20
	v_add_u32_e32 v21, 0x1000, v21
	v_lshl_add_u64 v[34:35], v[18:19], 2, s[28:29]
	s_or_b64 s[2:3], vcc, s[2:3]
	s_waitcnt lgkmcnt(0)
	global_store_dword v[34:35], v27, off sc1
	s_andn2_b64 exec, exec, s[2:3]
	s_cbranch_execnz .LBB1_69
	s_or_b64 exec, exec, s[2:3]

.LBB1_74:
	ds_read_b32 v10, v18 offset:19968
	v_ashrrev_i32_e32 v25, 31, v24
	v_lshlrev_b64 v[12:13], 7, v[24:25]
	s_waitcnt lgkmcnt(0)
	v_mul_f32_e32 v6, v10, v6
	v_mul_f32_e32 v7, v10, v7
	v_mul_f32_e32 v8, v10, v8
	v_mul_f32_e32 v9, v10, v9
	v_cvt_pk_f16_f32 v6, v6, v7
	v_cvt_pk_f16_f32 v7, v8, v9
	v_lshl_add_u64 v[8:9], v[0:1], 0, v[12:13]
	global_store_dwordx2 v[8:9], v[6:7], off sc1
.LBB1_75:
	s_or_b64 exec, exec, s[0:1]
	s_movk_i32 s0, 0xc40
	v_cmp_gt_u32_e32 vcc, s0, v32
	v_cmp_gt_i32_e64 s[0:1], s2, v22
	s_and_b64 s[0:1], vcc, s[0:1]
	s_and_saveexec_b64 s[2:3], s[0:1]
	s_cbranch_execz .LBB1_77
	v_lshlrev_b32_e32 v6, 2, v23
	ds_read_b32 v6, v6 offset:19456
	v_ashrrev_i32_e32 v23, 31, v22
	v_lshlrev_b64 v[8:9], 7, v[22:23]
	v_lshl_add_u64 v[0:1], v[0:1], 0, v[8:9]
	s_waitcnt lgkmcnt(0)
	v_mul_f32_e32 v2, v6, v2
	v_mul_f32_e32 v3, v6, v3
	v_mul_f32_e32 v4, v6, v4
	v_mul_f32_e32 v5, v6, v5
	v_cvt_pk_f16_f32 v2, v2, v3
	v_cvt_pk_f16_f32 v3, v4, v5
	global_store_dwordx2 v[0:1], v[2:3], off sc1

.LBB1_78:
	ds_read_b32 v20, v18 offset:19456
	v_ashrrev_i32_e32 v29, 31, v28
	v_lshlrev_b64 v[28:29], 7, v[28:29]
	s_waitcnt lgkmcnt(0)
	v_mul_f32_e32 v14, v20, v14
	v_mul_f32_e32 v15, v20, v15
	v_mul_f32_e32 v16, v20, v16
	v_mul_f32_e32 v17, v20, v17
	v_cvt_pk_f16_f32 v14, v14, v15
	v_cvt_pk_f16_f32 v15, v16, v17
	v_lshl_add_u64 v[16:17], v[0:1], 0, v[28:29]
	global_store_dwordx2 v[16:17], v[14:15], off sc1
	s_or_b64 exec, exec, s[0:1]
	v_cmp_gt_i32_e32 vcc, s2, v26
	s_and_saveexec_b64 s[0:1], vcc
	s_cbranch_execz .LBB1_73
.LBB1_79:
	ds_read_b32 v14, v18 offset:19712
	v_ashrrev_i32_e32 v27, 31, v26
	v_lshlrev_b64 v[16:17], 7, v[26:27]
	s_waitcnt lgkmcnt(0)
	v_mul_f32_e32 v10, v14, v10
	v_mul_f32_e32 v11, v14, v11
	v_mul_f32_e32 v12, v14, v12
	v_mul_f32_e32 v13, v14, v13
	v_cvt_pk_f16_f32 v10, v10, v11
	v_cvt_pk_f16_f32 v11, v12, v13
	v_lshl_add_u64 v[12:13], v[0:1], 0, v[16:17]
	global_store_dwordx2 v[12:13], v[10:11], off sc1
	s_or_b64 exec, exec, s[0:1]
	v_cmp_gt_i32_e32 vcc, s2, v24
	s_and_saveexec_b64 s[0:1], vcc
	s_cbranch_execnz .LBB1_74
	s_branch .LBB1_75

.LBB2_30:
	s_or_b64 exec, exec, s[0:1]
	s_mov_b32 s6, 0x437f0000
	v_div_scale_f32 v28, s[0:1], v27, v27, s6
	v_rcp_f32_e32 v29, v28
	v_div_scale_f32 v30, vcc, s6, v27, s6
	s_movk_i32 s0, 0x90
	v_fma_f32 v31, -v28, v29, 1.0
	v_fmac_f32_e32 v29, v31, v29
	v_mul_f32_e32 v31, v30, v29
	v_fma_f32 v32, -v28, v31, v30
	v_fmac_f32_e32 v31, v32, v29
	v_fma_f32 v28, -v28, v31, v30
	v_div_fmas_f32 v28, v28, v29, v31
	v_div_fixup_f32 v28, v28, v27, s6
	v_cmp_lt_f32_e32 vcc, 0, v27
	s_nop 1
	v_cndmask_b32_e32 v27, 0, v28, vcc
	v_fma_f32 v28, v27, v42, 0.5
	v_fma_f32 v29, v27, v41, 0.5
	v_fma_f32 v30, v27, v40, 0.5
	v_fma_f32 v31, v27, v37, 0.5
	v_cvt_u32_f32_e32 v28, v28
	v_cvt_u32_f32_e32 v29, v29
	v_cvt_u32_f32_e32 v30, v30
	v_cvt_u32_f32_e32 v31, v31
	v_fma_f32 v25, v27, v25, 0.5
	v_fma_f32 v20, v27, v20, 0.5
	v_lshl_or_b32 v28, v30, 8, v28
	v_lshl_or_b32 v29, v31, 8, v29
	v_fma_f32 v30, v27, v36, 0.5
	v_fma_f32 v31, v27, v35, 0.5
	v_cvt_u32_f32_e32 v25, v25
	v_fma_f32 v24, v27, v24, 0.5
	v_cvt_u32_f32_e32 v20, v20
	v_fma_f32 v19, v27, v19, 0.5
	v_fma_f32 v6, v27, v6, 0.5
	v_cvt_u32_f32_e32 v30, v30
	v_cvt_u32_f32_e32 v31, v31
	v_fma_f32 v32, v27, v34, 0.5
	v_fma_f32 v26, v27, v26, 0.5
	v_cvt_u32_f32_e32 v24, v24
	v_cvt_u32_f32_e32 v19, v19
	v_cvt_u32_f32_e32 v6, v6
	v_fma_f32 v4, v27, v4, 0.5
	v_fma_f32 v3, v27, v3, 0.5
	v_cvt_u32_f32_e32 v32, v32
	v_cvt_u32_f32_e32 v26, v26
	v_cvt_u32_f32_e32 v4, v4
	v_cvt_u32_f32_e32 v3, v3
	v_fma_f32 v2, v27, v2, 0.5
	v_cvt_u32_f32_e32 v2, v2
	v_lshl_or_b32 v20, v20, 8, v25
	v_lshl_or_b32 v28, v30, 16, v28
	v_lshl_or_b32 v29, v31, 16, v29
	v_lshl_or_b32 v19, v19, 8, v24
	v_lshl_or_b32 v6, v6, 16, v20
	v_lshl_or_b32 v28, v32, 24, v28
	v_lshl_or_b32 v26, v26, 24, v29
	v_mad_u32_u24 v29, v66, s0, v67
	v_lshl_or_b32 v4, v4, 16, v19
	v_lshl_or_b32 v3, v3, 24, v6
	v_lshl_or_b32 v2, v2, 24, v4
	ds_write2_b32 v29, v28, v3 offset1:2
	v_add_u32_e32 v3, 0x1000, v29
	ds_write2_b32 v3, v26, v2 offset0:128 offset1:130
	v_fma_f32 v2, v27, v5, 0.5
	v_fma_f32 v5, v27, v8, 0.5
	v_cvt_u32_f32_e32 v2, v2
	v_fma_f32 v4, v27, v7, 0.5
	v_cvt_u32_f32_e32 v5, v5
	v_fma_f32 v6, v27, v9, 0.5
	v_fma_f32 v7, v27, v18, 0.5
	v_cvt_u32_f32_e32 v4, v4
	v_cvt_u32_f32_e32 v6, v6
	v_cvt_u32_f32_e32 v7, v7
	v_fma_f32 v8, v27, v12, 0.5
	v_cvt_u32_f32_e32 v8, v8
	v_lshl_or_b32 v2, v5, 8, v2
	v_lshl_or_b32 v4, v6, 8, v4
	v_lshl_or_b32 v2, v7, 16, v2
	v_fma_f32 v5, v27, v10, 0.5
	v_fma_f32 v7, v27, v13, 0.5
	v_fma_f32 v9, v27, v21, 0.5
	v_lshl_or_b32 v4, v8, 16, v4
	v_cvt_u32_f32_e32 v5, v5
	v_fma_f32 v6, v27, v11, 0.5
	v_cvt_u32_f32_e32 v7, v7
	v_fma_f32 v8, v27, v14, 0.5
	v_cvt_u32_f32_e32 v9, v9
	v_fma_f32 v10, v27, v22, 0.5
	v_cvt_u32_f32_e32 v6, v6
	v_cvt_u32_f32_e32 v8, v8
	v_cvt_u32_f32_e32 v10, v10
	v_lshl_or_b32 v2, v5, 24, v2
	v_lshl_or_b32 v5, v9, 8, v7
	v_fma_f32 v7, v27, v15, 0.5
	v_lshl_or_b32 v4, v6, 24, v4
	v_lshl_or_b32 v6, v10, 8, v8
	v_cvt_u32_f32_e32 v7, v7
	v_fma_f32 v8, v27, v16, 0.5
	v_fma_f32 v9, v27, v23, 0.5
	v_cvt_u32_f32_e32 v8, v8
	v_cvt_u32_f32_e32 v9, v9
	v_fma_f32 v10, v27, v17, 0.5
	v_cvt_u32_f32_e32 v10, v10
	v_lshl_or_b32 v5, v7, 16, v5
	s_movk_i32 s0, 0x200
	v_lshl_or_b32 v6, v8, 16, v6
	v_lshl_or_b32 v5, v9, 24, v5
	v_cmp_gt_u32_e32 vcc, s0, v0
	v_lshl_or_b32 v6, v10, 24, v6
	ds_write2_b32 v29, v2, v5 offset0:4 offset1:6
	ds_write2_b32 v3, v4, v6 offset0:132 offset1:134
	s_waitcnt lgkmcnt(0)
	s_barrier
	s_and_saveexec_b64 s[0:1], vcc
	s_cbranch_execz .LBB2_35
	s_mov_b32 s6, 0xc350
	v_cmp_gt_i32_e32 vcc, s6, v72
	s_and_b64 s[2:3], s[2:3], vcc
	s_and_saveexec_b64 s[0:1], s[2:3]
	s_cbranch_execz .LBB2_33
	s_movk_i32 s2, 0x90
	v_mad_u32_u24 v0, v1, s2, v74
	ds_read_b128 v[0:3], v0
	v_ashrrev_i32_e32 v73, 31, v72
	v_lshlrev_b64 v[4:5], 7, v[72:73]
	v_mov_b32_e32 v75, 0
	v_lshl_add_u64 v[4:5], s[10:11], 0, v[4:5]
	v_lshl_add_u64 v[4:5], v[4:5], 0, v[74:75]
	s_waitcnt lgkmcnt(0)
	global_store_dwordx4 v[4:5], v[0:3], off sc1
.LBB2_33:
	s_or_b64 exec, exec, s[0:1]
	v_cmp_gt_i32_e32 vcc, s6, v70
	s_and_b64 s[0:1], s[4:5], vcc
	s_and_saveexec_b64 s[2:3], s[0:1]
	s_xor_b64 s[2:3], exec, s[2:3]
	s_cbranch_execz .LBB2_35
	s_movk_i32 s0, 0x90
	v_mad_u32_u24 v0, v71, s0, v74
	ds_read_b128 v[0:3], v0
	v_ashrrev_i32_e32 v71, 31, v70
	v_lshlrev_b64 v[4:5], 7, v[70:71]
	v_mov_b32_e32 v75, 0
	v_lshl_add_u64 v[4:5], s[10:11], 0, v[4:5]
	v_lshl_add_u64 v[4:5], v[4:5], 0, v[74:75]
	s_waitcnt lgkmcnt(0)
	global_store_dwordx4 v[4:5], v[0:3], off sc1
